# sel phase: next triple's LDS-DMA issued block by block at the top of each block iteration instead of all nine pieces right after the barrier
# speedup vs baseline: 1.0033x; 1.0027x over previous
; #define RING_BARRIER() do { asm volatile("s_waitcnt lgkmcnt(0)" ::: "memory"); __builtin_amdgcn_s_barrier(); asm volatile("" ::: "memory"); } while (0)
; template <bool DUMMY> __device__ __forceinline__ void sel_phase(Frame& F) {
;     ...
;         for (int p = 0; p < npair; ++p) {
;             u32x2 dnx = {0xffffffffu, 0u}; if (p + 1 < npair) dnx = PD[(p + 1) * 8 + F.wave];
;             asm volatile("s_waitcnt vmcnt(0)" ::: "memory"); RING_BARRIER();
;             const unsigned nj = (unsigned)__builtin_amdgcn_readfirstlane((int)dnx.x), nb = (unsigned)__builtin_amdgcn_readfirstlane((int)dnx.y);
;             if (p + 1 < npair && !(DUMMY && MK_EXP == 2)) { SEL_DMA3(nj, F.lds + ((p + 1) & 1) * 3 * SLOTS); }
.LBB0_1784:
	s_add_i32 s76, s36, 1
	s_cmp_lt_i32 s76, s59
	s_cselect_b64 s[12:13], -1, 0
	s_cselect_b32 s99, 1, 0
	s_cmp_ge_i32 s76, s59
	s_cbranch_scc1 .LBB0_1786
	s_lshl_b32 s37, s76, 6
	s_add_i32 s37, s84, s37
	v_mov_b32_e32 v18, s37
	ds_read_b64 v[84:85], v18
	s_branch .LBB0_1787

; #define RING_BARRIER() do { asm volatile("s_waitcnt lgkmcnt(0)" ::: "memory"); __builtin_amdgcn_s_barrier(); asm volatile("" ::: "memory"); } while (0)
; template <bool DUMMY> __device__ __forceinline__ void sel_phase(Frame& F) {
;     ...
;             u32x2 dnx = {0xffffffffu, 0u}; if (p + 1 < npair) dnx = PD[(p + 1) * 8 + F.wave];
;             asm volatile("s_waitcnt vmcnt(0)" ::: "memory"); RING_BARRIER();
;             const unsigned nj = (unsigned)__builtin_amdgcn_readfirstlane((int)dnx.x), nb = (unsigned)__builtin_amdgcn_readfirstlane((int)dnx.y);
;             if (p + 1 < npair && !(DUMMY && MK_EXP == 2)) { SEL_DMA3(nj, F.lds + ((p + 1) & 1) * 3 * SLOTS); }
.LBB0_1787:
	s_waitcnt vmcnt(0)
	s_waitcnt lgkmcnt(0)
	s_barrier
	s_waitcnt lgkmcnt(0)
	v_readfirstlane_b32 s60, v84
	s_andn2_b64 vcc, exec, s[12:13]
	v_readfirstlane_b32 s61, v85
	s_cbranch_vccnz .LBB0_1796
	s_bitcmp1_b32 s76, 0
	s_cselect_b32 s98, 0xe400, 0
	s_add_i32 s98, s85, s98

; #define LAS __attribute__((address_space(3)))
; __device__ __forceinline__ void ringS_dma(const RingSLane& R, const char* K8p, const char* VTp, LAS unsigned char* sb, int wave) {
;     __builtin_amdgcn_global_load_lds((const unsigned*)(K8p + R.so[0]), (LAS unsigned*)(sb + wave * 1024), 16, 0, 0);
;     __builtin_amdgcn_global_load_lds((const unsigned*)((wave == 0 ? K8p : VTp) + R.so[1]), (LAS unsigned*)(sb + (wave + 8) * 1024), 16, 0, 0);
;     if (wave <= 2) __builtin_amdgcn_global_load_lds((const unsigned*)(VTp + R.so[2]), (LAS unsigned*)(sb + (wave + 16) * 1024), 16, 0, 0);
; }
.LBB0_1799:
	s_cmp_eq_u32 s99, 0
	s_cbranch_scc1 .Lsel_nodma
	s_cmp_eq_u32 s37, 0
	s_cbranch_scc1 .Lsel_dodma
	s_add_i32 s12, s37, 23
	s_lshr_b32 s12, s60, s12
	s_bitcmp1_b32 s12, 0
	s_cbranch_scc0 .Lsel_nodma
.Lsel_dodma:
	s_lshr_b32 s12, s60, s36
	s_and_b32 s12, s12, 0xff
	s_lshl_b32 s12, s12, 13
	s_add_u32 s44, s62, s12
	s_addc_u32 s45, s63, 0
	s_add_u32 s12, s64, s12
	s_addc_u32 s13, s65, 0
	s_mul_i32 s97, s37, 0x4c00
	s_add_i32 s97, s98, s97
	s_and_b64 vcc, exec, s[16:17]
	v_lshl_add_u64 v[84:85], s[44:45], 0, v[102:103]
	s_mov_b32 m0, s97
	s_cselect_b32 s45, s45, s13
	s_cselect_b32 s44, s44, s12
	global_load_lds_dwordx4 v[84:85], off
	v_lshl_add_u64 v[84:85], s[44:45], 0, v[106:107]
	s_add_i32 m0, s97, 0x2000
	s_and_b64 vcc, exec, s[10:11]
	global_load_lds_dwordx4 v[84:85], off
	s_cbranch_vccnz .Lsel_nodma
	v_lshl_add_u64 v[84:85], s[12:13], 0, v[108:109]
	s_add_i32 m0, s97, 0x4000
	s_nop 0
	global_load_lds_dwordx4 v[84:85], off
